# MP0 wave-0 feature-chunk build: row-validity masks skipped by a scalar test unless the next tile reaches past nrows
# baseline (speedup 1.0000x reference)
.LBB5_14:
	v_or_b32_e32 v0, s33, v200
	ds_read_b128 v[142:145], v0 offset:0
	s_waitcnt lgkmcnt(4)
	s_nop 0
	v_mfma_f32_16x16x32_f16 v[134:137], v[114:117], v[134:137], v[166:169]
	ds_read_b128 v[146:149], v0 offset:0x1000
	s_waitcnt lgkmcnt(4)
	s_nop 0
	v_mfma_f32_16x16x32_f16 v[138:141], v[114:117], v[138:141], v[170:173]
	ds_read_b128 v[150:153], v0 offset:0x2000
	s_waitcnt lgkmcnt(4)
	s_nop 0
	v_mfma_f32_16x16x32_f16 v[154:157], v[114:117], v[158:161], v[174:177]
	ds_read_b128 v[158:161], v0 offset:0x3000
	s_waitcnt lgkmcnt(4)
	s_nop 0
	v_mfma_f32_16x16x32_f16 v[162:165], v[114:117], v[162:165], v[178:181]
	ds_read_b128 v[166:169], v205 offset:0
	s_waitcnt lgkmcnt(4)
	s_nop 0
	v_mfma_f32_16x16x32_f16 v[134:137], v[106:109], v[142:145], v[134:137]
	ds_read_b128 v[142:145], v205 offset:0x100
	s_waitcnt lgkmcnt(4)
	s_nop 0
	v_mfma_f32_16x16x32_f16 v[138:141], v[106:109], v[146:149], v[138:141]
	ds_read_b128 v[146:149], v205 offset:0x200
	s_waitcnt lgkmcnt(4)
	s_nop 0
	v_mfma_f32_16x16x32_f16 v[150:153], v[106:109], v[150:153], v[154:157]
	ds_read_b128 v[154:157], v205 offset:0x300
	s_waitcnt lgkmcnt(4)
	s_nop 0
	v_mfma_f32_16x16x32_f16 v[158:161], v[106:109], v[158:161], v[162:165]
	s_waitcnt lgkmcnt(3)
	s_nop 0
	v_mfma_f32_16x16x32_f16 v[134:137], v[102:105], v[166:169], v[134:137]
	s_waitcnt lgkmcnt(2)
	s_nop 0
	v_mfma_f32_16x16x32_f16 v[138:141], v[102:105], v[142:145], v[138:141]
	s_waitcnt lgkmcnt(1)
	s_nop 0
	v_mfma_f32_16x16x32_f16 v[142:145], v[102:105], v[146:149], v[150:153]
	s_waitcnt lgkmcnt(0)
	s_nop 0
	v_mfma_f32_16x16x32_f16 v[146:149], v[102:105], v[154:157], v[158:161]
	s_nop 1
	v_cvt_pk_f16_f32 v1, v136, v137
	v_pk_max_f16 v1, v1, 0
	v_cvt_pk_f16_f32 v0, v134, v135
	v_pk_max_f16 v0, v0, 0
	v_cvt_pk_f16_f32 v135, v140, v141
	v_pk_max_f16 v135, v135, 0
	v_cvt_pk_f16_f32 v134, v138, v139
	v_pk_max_f16 v134, v134, 0
	ds_write2st64_b64 v218, v[0:1], v[134:135] offset1:8
	v_cvt_pk_f16_f32 v1, v144, v145
	v_pk_max_f16 v1, v1, 0
	v_cvt_pk_f16_f32 v0, v142, v143
	v_pk_max_f16 v0, v0, 0
	s_lshl_b32 s34, s2, 14
	v_cvt_pk_f16_f32 v135, v148, v149
	v_pk_max_f16 v135, v135, 0
	v_cvt_pk_f16_f32 v134, v146, v147
	v_pk_max_f16 v134, v134, 0
	s_or_b32 s34, s34, 0x18000
	ds_write2st64_b64 v218, v[0:1], v[134:135] offset0:16 offset1:24
	v_or_b32_e32 v172, s34, v197
	v_or_b32_e32 v223, s34, v198
	v_or_b32_e32 v143, s34, v199
	v_or_b32_e32 v142, s34, v200
	v_add_u32_e32 v0, s34, v208
	s_xor_b32 s34, s2, 1
	s_waitcnt vmcnt(2) lgkmcnt(0)
	s_barrier
	ds_read_b128 v[134:137], v201 offset:0
	s_mul_i32 s37, s34, 0xc000
	ds_read_b128 v[138:141], v202 offset:0
	ds_read_b128 v[144:147], v203 offset:0
	ds_read_b128 v[148:151], v204 offset:0
	v_add_u32_e32 v1, s37, v209
	ds_read_b128 v[152:155], v1 offset:0
	ds_read_b128 v[156:159], v1 offset:0x4000
	ds_read_b128 v[160:163], v1 offset:0x8000
	ds_read_b128 v[164:167], v1 offset:0x400
	ds_read_b128 v[168:171], v1 offset:0x4400
	ds_read_b128 v[174:177], v1 offset:0x8400
	ds_read_b128 v[178:181], v172 offset:0
	s_waitcnt lgkmcnt(10)
	v_subrev_u32_e32 v186, 56, v215
	v_mfma_f32_16x16x32_f16 v[182:185], v[2:5], v[134:137], v[118:121]
	v_min_u32_e32 v225, s17, v186
	v_add_u32_e32 v224, s20, v216
	v_mov_b32_e32 v230, s16
	v_mfma_f32_16x16x32_f16 v[186:189], v[42:45], v[134:137], v[122:125]
	v_cmp_gt_u32_e32 vcc, s8, v224
	ds_read_b128 v[226:229], v223 offset:0
	s_waitcnt lgkmcnt(10)
	v_mfma_f32_16x16x32_f16 v[134:137], v[66:69], v[134:137], v[126:129]
	v_lshl_or_b32 v173, v196, 8, v190
	v_cndmask_b32_e32 v230, v230, v224, vcc
	v_lshlrev_b32_e32 v234, 5, v230
	v_mfma_f32_16x16x32_f16 v[182:185], v[6:9], v[138:141], v[182:185]
	v_add_u32_e32 v196, -8, v215
	v_min_u32_e32 v238, s17, v196
	v_subrev_u32_e32 v196, 52, v215
	v_mfma_f32_16x16x32_f16 v[186:189], v[46:49], v[138:141], v[186:189]
	v_add_u32_e32 v221, -4, v215
	v_min_u32_e32 v196, s18, v196
	v_min_u32_e32 v221, s18, v221
	v_mfma_f32_16x16x32_f16 v[230:233], v[70:73], v[138:141], v[134:137]
	global_load_dwordx4 v[134:137], v234, s[6:7]
	global_load_dwordx4 v[138:141], v234, s[6:7] offset:16
	ds_read_b128 v[234:237], v143 offset:0
	s_waitcnt lgkmcnt(10)
	v_lshl_or_b32 v242, v192, 8, v190
	v_mfma_f32_16x16x32_f16 v[182:185], v[50:53], v[144:147], v[182:185]
	global_load_dword v192, v196, s[4:5]
	v_subrev_u32_e32 v239, 48, v215
	global_load_dword v221, v221, s[4:5]
	v_mfma_f32_16x16x32_f16 v[186:189], v[18:21], v[144:147], v[186:189]
	v_min_u32_e32 v222, s19, v215
	v_min_u32_e32 v239, s19, v239
	v_lshl_or_b32 v241, v194, 8, v191
	v_mfma_f32_16x16x32_f16 v[144:147], v[74:77], v[144:147], v[230:233]
	global_load_dword v196, v239, s[4:5]
	ds_read_b128 v[230:233], v142 offset:0
	s_waitcnt lgkmcnt(10)
	global_load_dword v194, v222, s[4:5]
	s_add_i32 s2, s28, s3
	v_mfma_f32_16x16x32_f16 v[182:185], v[10:13], v[148:151], v[182:185]
	v_lshl_or_b32 v243, v193, 8, v190
	global_load_dword v193, v225, s[4:5]
	s_min_i32 s35, s2, s14
	v_mfma_f32_16x16x32_f16 v[186:189], v[58:61], v[148:151], v[186:189]
	global_load_dword v222, v238, s[4:5]
	s_lshl_b32 s35, s35, 14
	s_lshl_b32 s34, s34, 14
	v_mfma_f32_16x16x32_f16 v[148:151], v[90:93], v[148:151], v[144:147]
	s_add_i32 s36, s33, 0
	v_add_u32_e32 v1, s35, v210
	s_add_i32 s38, s25, s34
	s_add_i32 s39, s36, s21
	s_add_i32 s40, s26, s34
	s_add_i32 s34, s36, s23
	s_add_i32 m0, s39, 0x8000
	v_add_u32_e32 v240, s35, v211
	s_add_i32 s41, s34, 0x8000
	s_add_i32 s35, s39, 0x4000
	s_add_i32 s36, s22, s33
	v_add_u32_e32 v239, s37, v212
	ds_read_b128 v[144:147], v201 offset:0x1000
	s_waitcnt lgkmcnt(4)
	s_waitcnt lgkmcnt(5)
	s_nop 0
	v_pk_add_f16 v152, v152, v156
	v_pk_add_f16 v153, v153, v157
	v_pk_add_f16 v154, v154, v158
	v_pk_add_f16 v155, v155, v159
	v_pk_add_f16 v154, v154, v162
	v_pk_add_f16 v155, v155, v163
	v_pk_add_f16 v153, v153, v161
	v_pk_add_f16 v152, v152, v160
	ds_write_b128 v239, v[152:155]
	v_pk_add_f16 v152, v164, v168
	v_pk_add_f16 v153, v165, v169
	v_pk_add_f16 v154, v166, v170
	v_pk_add_f16 v155, v167, v171
	v_pk_add_f16 v154, v154, v176
	v_pk_add_f16 v155, v155, v177
	v_pk_add_f16 v153, v153, v175
	v_pk_add_f16 v152, v152, v174
	ds_write_b128 v239, v[152:155] offset:1024
	ds_read_b128 v[152:155], v202 offset:0x1000
	s_waitcnt lgkmcnt(4)
	global_load_lds_dwordx4 v173, s[12:13]
	s_mov_b32 m0, s38
	ds_read_b128 v[168:171], v203 offset:0x1000
	s_waitcnt lgkmcnt(4)
	v_mfma_f32_16x16x32_f16 v[182:185], v[14:17], v[178:181], v[182:185]
	global_load_lds_dwordx4 v1, s[12:13]
	ds_read_b128 v[174:177], v204 offset:0x1000
	v_mfma_f32_16x16x32_f16 v[186:189], v[22:25], v[178:181], v[186:189]
	s_waitcnt lgkmcnt(4)
	v_mfma_f32_16x16x32_f16 v[178:181], v[86:89], v[178:181], v[130:133]
	v_mfma_f32_16x16x32_f16 v[156:159], v[26:29], v[226:229], v[182:185]
	v_mfma_f32_16x16x32_f16 v[160:163], v[34:37], v[226:229], v[186:189]
	v_mfma_f32_16x16x32_f16 v[164:167], v[78:81], v[226:229], v[178:181]
	v_mfma_f32_16x16x32_f16 v[156:159], v[30:33], v[234:237], v[156:159]
	v_mfma_f32_16x16x32_f16 v[160:163], v[38:41], v[234:237], v[160:163]
	v_mfma_f32_16x16x32_f16 v[164:167], v[82:85], v[234:237], v[164:167]
	v_mfma_f32_16x16x32_f16 v[156:159], v[54:57], v[230:233], v[156:159]
	v_mfma_f32_16x16x32_f16 v[160:163], v[62:65], v[230:233], v[160:163]
	v_mfma_f32_16x16x32_f16 v[164:167], v[94:97], v[230:233], v[164:167]
	s_mov_b32 m0, s41
	ds_read_b64 v[234:235], v0 offset:0
	ds_read_b128 v[178:181], v172 offset:0x1000
	s_waitcnt lgkmcnt(5)
	ds_read_b128 v[186:189], v223 offset:0x1000
	s_waitcnt lgkmcnt(5)
	s_nop 4
	v_exp_f32_e32 v1, v156
	s_waitcnt lgkmcnt(2)
	ds_read_b128 v[230:233], v143 offset:0x1000
	s_waitcnt lgkmcnt(5)
	global_load_lds_dwordx4 v241, s[12:13]
	v_add_f32_e32 v1, 1.0, v1
	v_rcp_f32_e32 v1, v1
	v_exp_f32_e32 v156, v160
	v_mfma_f32_16x16x32_f16 v[182:185], v[2:5], v[144:147], v[118:121]
	v_add_u32_e32 v225, v206, v213
	v_fma_f32 v1, v1, v164, v148
	v_exp_f32_e32 v1, v1
	v_add_f32_e32 v148, 1.0, v156
	v_exp_f32_e32 v156, v157
	v_rcp_f32_e32 v148, v148
	v_add_f32_e32 v1, 1.0, v1
	v_rcp_f32_e32 v1, v1
	v_add_f32_e32 v156, 1.0, v156
	v_rcp_f32_e32 v156, v156
	v_mfma_f32_16x16x32_f16 v[226:229], v[42:45], v[144:147], v[122:125]
	v_fma_f32 v1, v1, -2.0, 1.0
	v_fma_f32 v1, -v148, v1, v1
	v_fma_mixlo_f16 v1, v148, v234, v1 op_sel_hi:[0,1,0]
	v_mfma_f32_16x16x32_f16 v[144:147], v[66:69], v[144:147], v[126:129]
	v_exp_f32_e32 v148, v161
	v_fma_f32 v149, v156, v165, v149
	v_exp_f32_e32 v149, v149
	v_mfma_f32_16x16x32_f16 v[182:185], v[6:9], v[152:155], v[182:185]
	v_add_f32_e32 v148, 1.0, v148
	v_rcp_f32_e32 v156, v148
	v_add_f32_e32 v148, 1.0, v149
	v_mfma_f32_16x16x32_f16 v[226:229], v[46:49], v[152:155], v[226:229]
	v_rcp_f32_e32 v157, v148
	v_add_u32_e32 v173, 0x1000, v225
	v_mfma_f32_16x16x32_f16 v[144:147], v[70:73], v[152:155], v[144:147]
	v_mfma_f32_16x16x32_f16 v[152:155], v[50:53], v[168:171], v[182:185]
	v_mfma_f32_16x16x32_f16 v[182:185], v[18:21], v[168:171], v[226:229]
	v_mfma_f32_16x16x32_f16 v[144:147], v[74:77], v[168:171], v[144:147]
	ds_read_b128 v[168:171], v142 offset:0x1000
	s_waitcnt lgkmcnt(5)
	s_nop 0
	v_mfma_f32_16x16x32_f16 v[152:155], v[10:13], v[174:177], v[152:155]
	v_mfma_f32_16x16x32_f16 v[182:185], v[58:61], v[174:177], v[182:185]
	v_mfma_f32_16x16x32_f16 v[146:149], v[90:93], v[174:177], v[144:147]
	s_nop 3
	v_fma_f32 v144, v157, -2.0, 1.0
	v_fma_f32 v144, -v156, v144, v144
	v_fma_mixlo_f16 v144, v156, v234, v144 op_sel:[0,1,0] op_sel_hi:[0,1,0]
	s_mov_b32 m0, s40
	ds_read_b128 v[174:177], v201 offset:0x2000
	s_waitcnt lgkmcnt(4)
	ds_read_b128 v[226:229], v202 offset:0x2000
	s_waitcnt lgkmcnt(4)
	v_exp_f32_e32 v145, v158
	global_load_lds_dwordx4 v240, s[12:13]
	v_exp_f32_e32 v156, v162
	v_add_f32_e32 v145, 1.0, v145
	v_rcp_f32_e32 v145, v145
	v_mfma_f32_16x16x32_f16 v[152:155], v[14:17], v[178:181], v[152:155]
	v_pack_b32_f16 v144, v1, v144
	v_fma_f32 v145, v145, v166, v150
	v_add_f32_e32 v150, 1.0, v156
	v_rcp_f32_e32 v234, v150
	v_exp_f32_e32 v150, v159
	v_mfma_f32_16x16x32_f16 v[182:185], v[22:25], v[178:181], v[182:185]
	v_exp_f32_e32 v145, v145
	v_add_f32_e32 v150, 1.0, v150
	v_mfma_f32_16x16x32_f16 v[178:181], v[86:89], v[178:181], v[130:133]
	v_rcp_f32_e32 v150, v150
	v_add_f32_e32 v145, 1.0, v145
	v_rcp_f32_e32 v145, v145
	v_mfma_f32_16x16x32_f16 v[182:185], v[34:37], v[186:189], v[182:185]
	v_fmac_f32_e32 v151, v150, v167
	v_fma_f32 v145, v145, -2.0, 1.0
	v_mfma_f32_16x16x32_f16 v[178:181], v[78:81], v[186:189], v[178:181]
	v_fma_f32 v145, -v234, v145, v145
	v_fma_mixlo_f16 v145, v234, v235, v145 op_sel_hi:[0,1,0]
	v_mfma_f32_16x16x32_f16 v[152:155], v[26:29], v[186:189], v[152:155]
	ds_read_b128 v[186:189], v203 offset:0x2000
	s_waitcnt lgkmcnt(4)
	ds_read_b128 v[164:167], v204 offset:0x2000
	s_waitcnt lgkmcnt(4)
	s_nop 0
	v_mfma_f32_16x16x32_f16 v[156:159], v[38:41], v[230:233], v[182:185]
	s_nop 2
	v_exp_f32_e32 v182, v163
	v_mfma_f32_16x16x32_f16 v[160:163], v[82:85], v[230:233], v[178:181]
	s_nop 2
	v_exp_f32_e32 v178, v151
	v_mfma_f32_16x16x32_f16 v[152:155], v[30:33], v[230:233], v[152:155]
	v_add_f32_e32 v179, 1.0, v182
	v_add_f32_e32 v178, 1.0, v178
	v_mfma_f32_16x16x32_f16 v[150:153], v[54:57], v[168:171], v[152:155]
	v_mfma_f32_16x16x32_f16 v[154:157], v[62:65], v[168:171], v[156:159]
	s_nop 2
	v_rcp_f32_e32 v158, v178
	v_rcp_f32_e32 v159, v179
	v_mfma_f32_16x16x32_f16 v[168:171], v[94:97], v[168:171], v[160:163]
	v_fma_f32 v158, v158, -2.0, 1.0
	v_fma_f32 v158, -v159, v158, v158
	v_fma_mixlo_f16 v158, v159, v235, v158 op_sel:[0,1,0] op_sel_hi:[0,1,0]
	s_nop 0
	v_pack_b32_f16 v145, v145, v158
	global_store_dwordx2 v173, v[144:145], s[0:1] nt
	s_mov_b32 m0, s36
	ds_read_b64 v[238:239], v0 offset:0x1000
	ds_read_b128 v[178:181], v172 offset:0x2000
	s_waitcnt lgkmcnt(5)
	ds_read_b128 v[182:185], v223 offset:0x2000
	s_waitcnt lgkmcnt(5)
	v_exp_f32_e32 v1, v150
	s_waitcnt lgkmcnt(2)
	ds_read_b128 v[234:237], v143 offset:0x2000
	s_waitcnt lgkmcnt(5)
	global_load_lds_dwordx4 v243, s[12:13]
	v_add_f32_e32 v1, 1.0, v1
	v_rcp_f32_e32 v1, v1
	v_exp_f32_e32 v145, v151
	v_mfma_f32_16x16x32_f16 v[158:161], v[2:5], v[174:177], v[118:121]
	v_exp_f32_e32 v144, v154
	v_fma_f32 v1, v1, v168, v146
	v_exp_f32_e32 v1, v1
	v_mfma_f32_16x16x32_f16 v[230:233], v[42:45], v[174:177], v[122:125]
	v_add_f32_e32 v145, 1.0, v145
	v_rcp_f32_e32 v145, v145
	v_add_f32_e32 v1, 1.0, v1
	v_mfma_f32_16x16x32_f16 v[174:177], v[66:69], v[174:177], v[126:129]
	v_add_f32_e32 v144, 1.0, v144
	v_rcp_f32_e32 v1, v1
	v_rcp_f32_e32 v144, v144
	v_mfma_f32_16x16x32_f16 v[158:161], v[6:9], v[226:229], v[158:161]
	v_fma_f32 v145, v145, v169, v147
	v_exp_f32_e32 v145, v145
	v_exp_f32_e32 v146, v155
	v_mfma_f32_16x16x32_f16 v[174:177], v[70:73], v[226:229], v[174:177]
	v_fma_f32 v1, v1, -2.0, 1.0
	v_fma_f32 v1, -v144, v1, v1
	v_fma_mixlo_f16 v240, v144, v238, v1 op_sel_hi:[0,1,0]
	v_mfma_f32_16x16x32_f16 v[230:233], v[46:49], v[226:229], v[230:233]
	v_add_f32_e32 v144, 1.0, v145
	v_add_f32_e32 v1, 1.0, v146
	v_rcp_f32_e32 v150, v144
	v_mfma_f32_16x16x32_f16 v[158:161], v[50:53], v[186:189], v[158:161]
	v_rcp_f32_e32 v1, v1
	v_add_u32_e32 v173, 0x2000, v225
	v_fma_f32 v150, v150, -2.0, 1.0
	v_mfma_f32_16x16x32_f16 v[174:177], v[74:77], v[186:189], v[174:177]
	v_fma_f32 v243, -v1, v150, v150
	v_mfma_f32_16x16x32_f16 v[226:229], v[18:21], v[186:189], v[230:233]
	ds_read_b128 v[186:189], v142 offset:0x2000
	s_waitcnt lgkmcnt(5)
	s_nop 0
	v_mfma_f32_16x16x32_f16 v[158:161], v[10:13], v[164:167], v[158:161]
	v_mfma_f32_16x16x32_f16 v[144:147], v[90:93], v[164:167], v[174:177]
	v_mfma_f32_16x16x32_f16 v[226:229], v[58:61], v[164:167], v[226:229]
	s_mov_b32 m0, s35
	ds_read_b128 v[230:233], v201 offset:0x3000
	s_waitcnt lgkmcnt(4)
	v_exp_f32_e32 v150, v152
	v_mfma_f32_16x16x32_f16 v[164:167], v[14:17], v[178:181], v[158:161]
	ds_read_b128 v[160:163], v202 offset:0x3000
	s_waitcnt lgkmcnt(4)
	global_load_lds_dwordx4 v242, s[12:13]
	v_exp_f32_e32 v154, v153
	v_add_f32_e32 v150, 1.0, v150
	v_rcp_f32_e32 v150, v150
	v_mfma_f32_16x16x32_f16 v[174:177], v[22:25], v[178:181], v[226:229]
	v_add_f32_e32 v154, 1.0, v154
	v_rcp_f32_e32 v154, v154
	v_exp_f32_e32 v151, v156
	v_mfma_f32_16x16x32_f16 v[178:181], v[86:89], v[178:181], v[130:133]
	v_fma_f32 v148, v150, v170, v148
	v_exp_f32_e32 v148, v148
	v_fmac_f32_e32 v149, v154, v171
	v_mfma_f32_16x16x32_f16 v[226:229], v[26:29], v[182:185], v[164:167]
	v_exp_f32_e32 v149, v149
	v_add_f32_e32 v150, 1.0, v151
	v_rcp_f32_e32 v241, v150
	v_mfma_f32_16x16x32_f16 v[174:177], v[34:37], v[182:185], v[174:177]
	v_add_f32_e32 v148, 1.0, v148
	ds_read_b128 v[164:167], v203 offset:0x3000
	s_waitcnt lgkmcnt(4)
	v_mfma_f32_16x16x32_f16 v[178:181], v[78:81], v[182:185], v[178:181]
	v_exp_f32_e32 v155, v157
	v_rcp_f32_e32 v148, v148
	v_add_f32_e32 v149, 1.0, v149
	v_mfma_f32_16x16x32_f16 v[150:153], v[30:33], v[234:237], v[226:229]
	v_rcp_f32_e32 v149, v149
	ds_read_b128 v[168:171], v204 offset:0x3000
	s_waitcnt lgkmcnt(4)
	v_mfma_f32_16x16x32_f16 v[174:177], v[38:41], v[234:237], v[174:177]
	v_fma_f32 v148, v148, -2.0, 1.0
	v_fma_f32 v148, -v241, v148, v148
	v_fma_mixlo_f16 v241, v241, v239, v148 op_sel_hi:[0,1,0]
	v_mfma_f32_16x16x32_f16 v[178:181], v[82:85], v[234:237], v[178:181]
	v_fma_mixhi_f16 v240, v1, v238, v243 op_sel:[0,1,0] op_sel_hi:[0,1,0]
	v_mfma_f32_16x16x32_f16 v[156:159], v[54:57], v[186:189], v[150:153]
	s_nop 2
	v_add_f32_e32 v150, 1.0, v155
	v_mfma_f32_16x16x32_f16 v[152:155], v[62:65], v[186:189], v[174:177]
	s_nop 2
	v_rcp_f32_e32 v174, v150
	v_fma_f32 v175, v149, -2.0, 1.0
	v_mfma_f32_16x16x32_f16 v[148:151], v[94:97], v[186:189], v[178:181]
	v_fma_f32 v175, -v174, v175, v175
	v_fma_mixhi_f16 v241, v174, v239, v175 op_sel:[0,1,0] op_sel_hi:[0,1,0]
	global_store_dwordx2 v173, v[240:241], s[0:1] nt
	ds_read_b64 v[188:189], v0 offset:0x2000
	ds_read_b64 v[0:1], v0 offset:0x3000
	ds_read_b128 v[172:175], v172 offset:0x3000
	s_waitcnt lgkmcnt(6)
	s_andn2_b64 vcc, exec, s[10:11]
	v_mfma_f32_16x16x32_f16 v[180:183], v[2:5], v[230:233], v[118:121]
	s_waitcnt vmcnt(14)
	v_mfma_f32_16x16x32_f16 v[176:179], v[42:45], v[230:233], v[122:125]
	v_mfma_f32_16x16x32_f16 v[184:187], v[66:69], v[230:233], v[126:129]
	s_cbranch_vccnz .LBB5_11
	v_cvt_pk_f16_f32 v226, v134, v135
	v_cvt_pk_f16_f32 v227, v136, v137
	v_cvt_pk_f16_f32 v228, v138, v139
	v_cvt_pk_f16_f32 v229, v140, v141
	s_add_i32 s46, s20, s30
	s_add_i32 s46, s46, 63
	s_cmp_lt_i32 s46, s8
	s_cbranch_scc1 .Lmp0_fb_nomask
	v_cmp_gt_i32_e32 vcc, s8, v224
	s_nop 1
	v_cndmask_b32_e32 v226, 0, v226, vcc
	v_cndmask_b32_e32 v227, 0, v227, vcc
	v_cndmask_b32_e32 v228, 0, v228, vcc
	v_cndmask_b32_e32 v229, 0, v229, vcc
.Lmp0_fb_nomask:
	ds_write_b128 v220, v[226:229]
	s_branch .LBB5_11

	.amdhsa_kernel _Z10mp2_kernelILb0ELi0EEvPKDF16_PDF16_PKiPKfPKDv8_DF16_S6_S6_ii
		.amdhsa_group_segment_fixed_size 0
		.amdhsa_private_segment_fixed_size 0
		.amdhsa_kernarg_size 320
		.amdhsa_user_sgpr_count 2
		.amdhsa_user_sgpr_dispatch_ptr 0
		.amdhsa_user_sgpr_queue_ptr 0
		.amdhsa_user_sgpr_kernarg_segment_ptr 1
		.amdhsa_user_sgpr_dispatch_id 0
		.amdhsa_user_sgpr_kernarg_preload_length 0
		.amdhsa_user_sgpr_kernarg_preload_offset 0
		.amdhsa_user_sgpr_private_segment_size 0
		.amdhsa_uses_dynamic_stack 0
		.amdhsa_enable_private_segment 0
		.amdhsa_system_sgpr_workgroup_id_x 1
		.amdhsa_system_sgpr_workgroup_id_y 0
		.amdhsa_system_sgpr_workgroup_id_z 0
		.amdhsa_system_sgpr_workgroup_info 0
		.amdhsa_system_vgpr_workitem_id 0
		.amdhsa_next_free_vgpr 244
		.amdhsa_next_free_sgpr 48
		.amdhsa_accum_offset 244
		.amdhsa_reserve_vcc 1
		.amdhsa_float_round_mode_32 0
		.amdhsa_float_round_mode_16_64 0
		.amdhsa_float_denorm_mode_32 3
		.amdhsa_float_denorm_mode_16_64 3
		.amdhsa_dx10_clamp 1
		.amdhsa_ieee_mode 1
		.amdhsa_fp16_overflow 0
		.amdhsa_tg_split 0
		.amdhsa_exception_fp_ieee_invalid_op 0
		.amdhsa_exception_fp_denorm_src 0
		.amdhsa_exception_fp_ieee_div_zero 0
		.amdhsa_exception_fp_ieee_overflow 0
		.amdhsa_exception_fp_ieee_underflow 0
		.amdhsa_exception_fp_ieee_inexact 0
		.amdhsa_exception_int_div_zero 0
	.end_amdhsa_kernel

amdhsa.kernels:
  - .agpr_count:     0
    .args:
      - .actual_access:  write_only
        .address_space:  global
        .offset:         0
        .size:           8
        .value_kind:     global_buffer
      - .actual_access:  read_only
        .address_space:  global
        .offset:         8
        .size:           8
        .value_kind:     global_buffer
      - .actual_access:  read_only
        .address_space:  global
        .offset:         16
        .size:           8
        .value_kind:     global_buffer
      - .actual_access:  read_only
        .address_space:  global
        .offset:         24
        .size:           8
        .value_kind:     global_buffer
      - .actual_access:  read_only
        .address_space:  global
        .offset:         32
        .size:           8
        .value_kind:     global_buffer
      - .actual_access:  read_only
        .address_space:  global
        .offset:         40
        .size:           8
        .value_kind:     global_buffer
      - .actual_access:  read_only
        .address_space:  global
        .offset:         48
        .size:           8
        .value_kind:     global_buffer
      - .actual_access:  read_only
        .address_space:  global
        .offset:         56
        .size:           8
        .value_kind:     global_buffer
      - .actual_access:  read_only
        .address_space:  global
        .offset:         64
        .size:           8
        .value_kind:     global_buffer
      - .actual_access:  read_only
        .address_space:  global
        .offset:         72
        .size:           8
        .value_kind:     global_buffer
    .group_segment_fixed_size: 0
    .kernarg_segment_align: 8
    .kernarg_segment_size: 80
    .language:       OpenCL C
    .language_version:
      - 2
      - 0
    .max_flat_workgroup_size: 64
    .name:           _Z11prep_kernelPDv8_DF16_PKfS2_S2_S2_S2_S2_S2_S2_S2_
    .private_segment_fixed_size: 0
    .sgpr_count:     20
    .sgpr_spill_count: 0
    .symbol:         _Z11prep_kernelPDv8_DF16_PKfS2_S2_S2_S2_S2_S2_S2_S2_.kd
    .uniform_work_group_size: 1
    .uses_dynamic_stack: false
    .vgpr_count:     18
    .vgpr_spill_count: 0
    .wavefront_size: 64
  - .agpr_count:     0
    .args:
      - .actual_access:  read_only
        .address_space:  global
        .offset:         0
        .size:           8
        .value_kind:     global_buffer
      - .actual_access:  read_only
        .address_space:  global
        .offset:         8
        .size:           8
        .value_kind:     global_buffer
      - .actual_access:  write_only
        .address_space:  global
        .offset:         16
        .size:           8
        .value_kind:     global_buffer
    .group_segment_fixed_size: 0
    .kernarg_segment_align: 8
    .kernarg_segment_size: 24
    .language:       OpenCL C
    .language_version:
      - 2
      - 0
    .max_flat_workgroup_size: 256
    .name:           _Z11init_kernelPKfS0_PDF16_
    .private_segment_fixed_size: 0
    .sgpr_count:     16
    .sgpr_spill_count: 0
    .symbol:         _Z11init_kernelPKfS0_PDF16_.kd
    .uniform_work_group_size: 1
    .uses_dynamic_stack: false
    .vgpr_count:     118
    .vgpr_spill_count: 0
    .wavefront_size: 64
  - .agpr_count:     0
    .args:
      - .actual_access:  read_only
        .address_space:  global
        .offset:         0
        .size:           8
        .value_kind:     global_buffer
      - .actual_access:  write_only
        .address_space:  global
        .offset:         8
        .size:           8
        .value_kind:     global_buffer
      - .actual_access:  read_only
        .address_space:  global
        .offset:         16
        .size:           8
        .value_kind:     global_buffer
      - .actual_access:  read_only
        .address_space:  global
        .offset:         24
        .size:           8
        .value_kind:     global_buffer
      - .actual_access:  read_only
        .address_space:  global
        .offset:         32
        .size:           8
        .value_kind:     global_buffer
      - .actual_access:  read_only
        .address_space:  global
        .offset:         40
        .size:           8
        .value_kind:     global_buffer
      - .actual_access:  read_only
        .address_space:  global
        .offset:         48
        .size:           8
        .value_kind:     global_buffer
      - .offset:         56
        .size:           4
        .value_kind:     by_value
      - .offset:         64
        .size:           4
        .value_kind:     hidden_block_count_x
      - .offset:         68
        .size:           4
        .value_kind:     hidden_block_count_y
      - .offset:         72
        .size:           4
        .value_kind:     hidden_block_count_z
      - .offset:         76
        .size:           2
        .value_kind:     hidden_group_size_x
      - .offset:         78
        .size:           2
        .value_kind:     hidden_group_size_y
      - .offset:         80
        .size:           2
        .value_kind:     hidden_group_size_z
      - .offset:         82
        .size:           2
        .value_kind:     hidden_remainder_x
      - .offset:         84
        .size:           2
        .value_kind:     hidden_remainder_y
      - .offset:         86
        .size:           2
        .value_kind:     hidden_remainder_z
      - .offset:         104
        .size:           8
        .value_kind:     hidden_global_offset_x
      - .offset:         112
        .size:           8
        .value_kind:     hidden_global_offset_y
      - .offset:         120
        .size:           8
        .value_kind:     hidden_global_offset_z
      - .offset:         128
        .size:           2
        .value_kind:     hidden_grid_dims
      - .offset:         184
        .size:           4
        .value_kind:     hidden_dynamic_lds_size
    .group_segment_fixed_size: 0
    .kernarg_segment_align: 8
    .kernarg_segment_size: 320
    .language:       OpenCL C
    .language_version:
      - 2
      - 0
    .max_flat_workgroup_size: 512
    .name:           _Z12xproj_kernelPKDF16_PDF16_PKDv8_DF16_PKfS6_S6_S6_i
    .private_segment_fixed_size: 0
    .sgpr_count:     30
    .sgpr_spill_count: 0
    .symbol:         _Z12xproj_kernelPKDF16_PDF16_PKDv8_DF16_PKfS6_S6_S6_i.kd
    .uniform_work_group_size: 1
    .uses_dynamic_stack: false
    .vgpr_count:     16
    .vgpr_spill_count: 0
    .wavefront_size: 64
  - .agpr_count:     0
    .args:
      - .actual_access:  read_only
        .address_space:  global
        .offset:         0
        .size:           8
        .value_kind:     global_buffer
      - .actual_access:  read_only
        .address_space:  global
        .offset:         8
        .size:           8
        .value_kind:     global_buffer
      - .actual_access:  write_only
        .address_space:  global
        .offset:         16
        .size:           8
        .value_kind:     global_buffer
    .group_segment_fixed_size: 5120
    .kernarg_segment_align: 8
    .kernarg_segment_size: 24
    .language:       OpenCL C
    .language_version:
      - 2
      - 0
    .max_flat_workgroup_size: 1024
    .name:           _Z11lstm_kernelPKDF16_PKDv8_DF16_Pf
    .private_segment_fixed_size: 0
    .sgpr_count:     18
    .sgpr_spill_count: 0
    .symbol:         _Z11lstm_kernelPKDF16_PKDv8_DF16_Pf.kd
    .uniform_work_group_size: 1
    .uses_dynamic_stack: false
    .vgpr_count:     52
    .vgpr_spill_count: 0
    .wavefront_size: 64
  - .agpr_count:     0
    .args:
      - .actual_access:  read_only
        .address_space:  global
        .offset:         0
        .size:           8
        .value_kind:     global_buffer
      - .actual_access:  read_only
        .address_space:  global
        .offset:         8
        .size:           8
        .value_kind:     global_buffer
      - .actual_access:  write_only
        .address_space:  global
        .offset:         16
        .size:           8
        .value_kind:     global_buffer
    .group_segment_fixed_size: 36096
    .kernarg_segment_align: 8
    .kernarg_segment_size: 24
    .language:       OpenCL C
    .language_version:
      - 2
      - 0
    .max_flat_workgroup_size: 256
    .name:           _Z12lstm2_kernelPKDF16_PKDv8_DF16_Pf
    .private_segment_fixed_size: 0
    .sgpr_count:     38
    .sgpr_spill_count: 0
    .symbol:         _Z12lstm2_kernelPKDF16_PKDv8_DF16_Pf.kd
    .uniform_work_group_size: 1
    .uses_dynamic_stack: false
    .vgpr_count:     252
    .vgpr_spill_count: 0
    .wavefront_size: 64
  - .agpr_count:     0
    .args:
      - .address_space:  global
        .offset:         0
        .size:           8
        .value_kind:     global_buffer
      - .actual_access:  write_only
        .address_space:  global
        .offset:         8
        .size:           8
        .value_kind:     global_buffer
      - .address_space:  global
        .offset:         16
        .size:           8
        .value_kind:     global_buffer
      - .address_space:  global
        .offset:         24
        .size:           8
        .value_kind:     global_buffer
      - .actual_access:  read_only
        .address_space:  global
        .offset:         32
        .size:           8
        .value_kind:     global_buffer
      - .actual_access:  read_only
        .address_space:  global
        .offset:         40
        .size:           8
        .value_kind:     global_buffer
      - .actual_access:  read_only
        .address_space:  global
        .offset:         48
        .size:           8
        .value_kind:     global_buffer
      - .offset:         56
        .size:           4
        .value_kind:     by_value
      - .offset:         60
        .size:           4
        .value_kind:     by_value
      - .offset:         64
        .size:           4
        .value_kind:     hidden_block_count_x
      - .offset:         68
        .size:           4
        .value_kind:     hidden_block_count_y
      - .offset:         72
        .size:           4
        .value_kind:     hidden_block_count_z
      - .offset:         76
        .size:           2
        .value_kind:     hidden_group_size_x
      - .offset:         78
        .size:           2
        .value_kind:     hidden_group_size_y
      - .offset:         80
        .size:           2
        .value_kind:     hidden_group_size_z
      - .offset:         82
        .size:           2
        .value_kind:     hidden_remainder_x
      - .offset:         84
        .size:           2
        .value_kind:     hidden_remainder_y
      - .offset:         86
        .size:           2
        .value_kind:     hidden_remainder_z
      - .offset:         104
        .size:           8
        .value_kind:     hidden_global_offset_x
      - .offset:         112
        .size:           8
        .value_kind:     hidden_global_offset_y
      - .offset:         120
        .size:           8
        .value_kind:     hidden_global_offset_z
      - .offset:         128
        .size:           2
        .value_kind:     hidden_grid_dims
      - .offset:         184
        .size:           4
        .value_kind:     hidden_dynamic_lds_size
    .group_segment_fixed_size: 0
    .kernarg_segment_align: 8
    .kernarg_segment_size: 320
    .language:       OpenCL C
    .language_version:
      - 2
      - 0
    .max_flat_workgroup_size: 512
    .name:           _Z10mp2_kernelILb0ELi0EEvPKDF16_PDF16_PKiPKfPKDv8_DF16_S6_S6_ii
    .private_segment_fixed_size: 0
    .sgpr_count:     54
    .sgpr_spill_count: 0
    .symbol:         _Z10mp2_kernelILb0ELi0EEvPKDF16_PDF16_PKiPKfPKDv8_DF16_S6_S6_ii.kd
    .uniform_work_group_size: 1
    .uses_dynamic_stack: false
    .vgpr_count:     244
    .vgpr_spill_count: 0
    .wavefront_size: 64
  - .agpr_count:     0
    .args:
      - .actual_access:  read_only
        .address_space:  global
        .offset:         0
        .size:           8
        .value_kind:     global_buffer
      - .actual_access:  write_only
        .address_space:  global
        .offset:         8
        .size:           8
        .value_kind:     global_buffer
      - .address_space:  global
        .offset:         16
        .size:           8
        .value_kind:     global_buffer
      - .address_space:  global
        .offset:         24
        .size:           8
        .value_kind:     global_buffer
      - .actual_access:  read_only
        .address_space:  global
        .offset:         32
        .size:           8
        .value_kind:     global_buffer
      - .actual_access:  read_only
        .address_space:  global
        .offset:         40
        .size:           8
        .value_kind:     global_buffer
      - .actual_access:  read_only
        .address_space:  global
        .offset:         48
        .size:           8
        .value_kind:     global_buffer
      - .offset:         56
        .size:           4
        .value_kind:     by_value
      - .offset:         60
        .size:           4
        .value_kind:     by_value
      - .offset:         64
        .size:           4
        .value_kind:     hidden_block_count_x
      - .offset:         68
        .size:           4
        .value_kind:     hidden_block_count_y
      - .offset:         72
        .size:           4
        .value_kind:     hidden_block_count_z
      - .offset:         76
        .size:           2
        .value_kind:     hidden_group_size_x
      - .offset:         78
        .size:           2
        .value_kind:     hidden_group_size_y
      - .offset:         80
        .size:           2
        .value_kind:     hidden_group_size_z
      - .offset:         82
        .size:           2
        .value_kind:     hidden_remainder_x
      - .offset:         84
        .size:           2
        .value_kind:     hidden_remainder_y
      - .offset:         86
        .size:           2
        .value_kind:     hidden_remainder_z
      - .offset:         104
        .size:           8
        .value_kind:     hidden_global_offset_x
      - .offset:         112
        .size:           8
        .value_kind:     hidden_global_offset_y
      - .offset:         120
        .size:           8
        .value_kind:     hidden_global_offset_z
      - .offset:         128
        .size:           2
        .value_kind:     hidden_grid_dims
      - .offset:         184
        .size:           4
        .value_kind:     hidden_dynamic_lds_size
    .group_segment_fixed_size: 0
    .kernarg_segment_align: 8
    .kernarg_segment_size: 320
    .language:       OpenCL C
    .language_version:
      - 2
      - 0
    .max_flat_workgroup_size: 512
    .name:           _Z10mp2_kernelILb0ELi1EEvPKDF16_PDF16_PKiPKfPKDv8_DF16_S6_S6_ii
    .private_segment_fixed_size: 0
    .sgpr_count:     30
    .sgpr_spill_count: 0
    .symbol:         _Z10mp2_kernelILb0ELi1EEvPKDF16_PDF16_PKiPKfPKDv8_DF16_S6_S6_ii.kd
    .uniform_work_group_size: 1
    .uses_dynamic_stack: false
    .vgpr_count:     234
    .vgpr_spill_count: 0
    .wavefront_size: 64
  - .agpr_count:     0
    .args:
      - .address_space:  global
        .offset:         0
        .size:           8
        .value_kind:     global_buffer
      - .actual_access:  write_only
        .address_space:  global
        .offset:         8
        .size:           8
        .value_kind:     global_buffer
      - .actual_access:  read_only
        .address_space:  global
        .offset:         16
        .size:           8
        .value_kind:     global_buffer
      - .actual_access:  read_only
        .address_space:  global
        .offset:         24
        .size:           8
        .value_kind:     global_buffer
      - .actual_access:  read_only
        .address_space:  global
        .offset:         32
        .size:           8
        .value_kind:     global_buffer
      - .actual_access:  read_only
        .address_space:  global
        .offset:         40
        .size:           8
        .value_kind:     global_buffer
      - .actual_access:  read_only
        .address_space:  global
        .offset:         48
        .size:           8
        .value_kind:     global_buffer
      - .offset:         56
        .size:           4
        .value_kind:     by_value
      - .offset:         60
        .size:           4
        .value_kind:     by_value
      - .offset:         64
        .size:           4
        .value_kind:     hidden_block_count_x
      - .offset:         68
        .size:           4
        .value_kind:     hidden_block_count_y
      - .offset:         72
        .size:           4
        .value_kind:     hidden_block_count_z
      - .offset:         76
        .size:           2
        .value_kind:     hidden_group_size_x
      - .offset:         78
        .size:           2
        .value_kind:     hidden_group_size_y
      - .offset:         80
        .size:           2
        .value_kind:     hidden_group_size_z
      - .offset:         82
        .size:           2
        .value_kind:     hidden_remainder_x
      - .offset:         84
        .size:           2
        .value_kind:     hidden_remainder_y
      - .offset:         86
        .size:           2
        .value_kind:     hidden_remainder_z
      - .offset:         104
        .size:           8
        .value_kind:     hidden_global_offset_x
      - .offset:         112
        .size:           8
        .value_kind:     hidden_global_offset_y
      - .offset:         120
        .size:           8
        .value_kind:     hidden_global_offset_z
      - .offset:         128
        .size:           2
        .value_kind:     hidden_grid_dims
      - .offset:         184
        .size:           4
        .value_kind:     hidden_dynamic_lds_size
    .group_segment_fixed_size: 0
    .kernarg_segment_align: 8
    .kernarg_segment_size: 320
    .language:       OpenCL C
    .language_version:
      - 2
      - 0
    .max_flat_workgroup_size: 512
    .name:           _Z9mp_kernelILi1EEvPKDF16_PDF16_PKiPKfPKDv8_DF16_S6_S6_ii
    .private_segment_fixed_size: 0
    .sgpr_count:     46
    .sgpr_spill_count: 0
    .symbol:         _Z9mp_kernelILi1EEvPKDF16_PDF16_PKiPKfPKDv8_DF16_S6_S6_ii.kd
    .uniform_work_group_size: 1
    .uses_dynamic_stack: false
    .vgpr_count:     70
    .vgpr_spill_count: 0
    .wavefront_size: 64
  - .agpr_count:     0
    .args:
      - .address_space:  global
        .offset:         0
        .size:           8
        .value_kind:     global_buffer
      - .actual_access:  write_only
        .address_space:  global
        .offset:         8
        .size:           8
        .value_kind:     global_buffer
      - .address_space:  global
        .offset:         16
        .size:           8
        .value_kind:     global_buffer
      - .address_space:  global
        .offset:         24
        .size:           8
        .value_kind:     global_buffer
      - .actual_access:  read_only
        .address_space:  global
        .offset:         32
        .size:           8
        .value_kind:     global_buffer
      - .actual_access:  read_only
        .address_space:  global
        .offset:         40
        .size:           8
        .value_kind:     global_buffer
      - .actual_access:  read_only
        .address_space:  global
        .offset:         48
        .size:           8
        .value_kind:     global_buffer
      - .offset:         56
        .size:           4
        .value_kind:     by_value
      - .offset:         60
        .size:           4
        .value_kind:     by_value
      - .offset:         64
        .size:           4
        .value_kind:     hidden_block_count_x
      - .offset:         68
        .size:           4
        .value_kind:     hidden_block_count_y
      - .offset:         72
        .size:           4
        .value_kind:     hidden_block_count_z
      - .offset:         76
        .size:           2
        .value_kind:     hidden_group_size_x
      - .offset:         78
        .size:           2
        .value_kind:     hidden_group_size_y
      - .offset:         80
        .size:           2
        .value_kind:     hidden_group_size_z
      - .offset:         82
        .size:           2
        .value_kind:     hidden_remainder_x
      - .offset:         84
        .size:           2
        .value_kind:     hidden_remainder_y
      - .offset:         86
        .size:           2
        .value_kind:     hidden_remainder_z
      - .offset:         104
        .size:           8
        .value_kind:     hidden_global_offset_x
      - .offset:         112
        .size:           8
        .value_kind:     hidden_global_offset_y
      - .offset:         120
        .size:           8
        .value_kind:     hidden_global_offset_z
      - .offset:         128
        .size:           2
        .value_kind:     hidden_grid_dims
      - .offset:         184
        .size:           4
        .value_kind:     hidden_dynamic_lds_size
    .group_segment_fixed_size: 0
    .kernarg_segment_align: 8
    .kernarg_segment_size: 320
    .language:       OpenCL C
    .language_version:
      - 2
      - 0
    .max_flat_workgroup_size: 512
    .name:           _Z10mp2_kernelILb0ELi2EEvPKDF16_PDF16_PKiPKfPKDv8_DF16_S6_S6_ii
    .private_segment_fixed_size: 0
    .sgpr_count:     32
    .sgpr_spill_count: 0
    .symbol:         _Z10mp2_kernelILb0ELi2EEvPKDF16_PDF16_PKiPKfPKDv8_DF16_S6_S6_ii.kd
    .uniform_work_group_size: 1
    .uses_dynamic_stack: false
    .vgpr_count:     99
    .vgpr_spill_count: 0
    .wavefront_size: 64
